# routed gate/up epilogue re-emitted: scales folded into MFMA block scales, eight silu chains interleaved per row group (bit-identical outputs)
# speedup vs baseline: 1.0425x; 1.0040x over previous
; #define PG8_STAGE(bufoff, gbase, voff) do { _Pragma("unroll") for (int _i = 0; _i < 2; ++_i) \
;         __builtin_amdgcn_global_load_lds((const unsigned*)((const char*)(gbase) + (voff)[_i]), (PG8_LAS unsigned*)(lds + (bufoff) + ldsw + _i * 8192), 16, 0, 0); } while (0)
; #define PG8_STAGE_A(bufoff, gbase, h, nx) do { if constexpr (Sched::GATHER) { unsigned _v[2]; _Pragma("unroll") for (int _i = 0; _i < 2; ++_i) _v[_i] = (nx) ? vAn[h][_i] : vA[h][_i]; PG8_STAGE(bufoff, gbase, _v); } \
;         else { PG8_STAGE(bufoff, (gbase) + (h) * hstep, voffA); } } while (0)
; #define PG8_WAIT_V(n) asm volatile("s_waitcnt vmcnt(" #n ")" ::: "memory")
; #define PG8_BAR __builtin_amdgcn_s_barrier()
; template <class Epi, class Sched, bool ALIGN_EPI = false, bool SP2 = false, bool FP8 = false>
; __device__ __forceinline__ void gemm_phase(PG8_LAS unsigned char* lds, const Gemm g, const Sched& S, const Epi& E) {
;     ...
;         PG8_STAGE(PG8_SB(0, 0), cB, voffB); PG8_STAGE(PG8_SB(0, 1), cB + hstep, voffB); PG8_STAGE_A(PG8_SA(0, 0), cA, 0, false); PG8_STAGE_A(PG8_SA(0, 1), cA, 1, false);
;         if (wr == 1) PG8_BAR;
;         PG8_WAIT_V(2); PG8_BAR;
;         PG8_STAGE(PG8_SB(1, 0), cB + kstep, voffB); PG8_STAGE_A(PG8_SA(1, 0), cA + kstep, 0, false); PG8_STAGE(PG8_SB(1, 1), cB + hstep + kstep, voffB);
;         PG8_WAIT_V(6); PG8_BAR;
;     __device__ __forceinline__ void operator()(const f32x4 (&acc)[2][2][4][2], const Unit& u, int wr, int wc, int fr, int fq) const {
;         const int r0 = wr * 64 + fr, col0 = (u.pn & 1) * 128 + wc * 32 + 8 * fq;
; #pragma unroll
;         for (int ai = 0; ai < 2; ++ai)
; #pragma unroll
;             for (int m = 0; m < 4; ++m) { const int r = r0 + ai * 128 + m * 16;
;                 if (r < u.aux1) { const int pid = list[u.aux0 + r]; float o[8];
.LBB0_1215:
	s_add_u32 s20, s0, 0x59a00000
	s_addc_u32 s21, s1, 0
	s_lshl_b32 s18, s18, 5
	s_and_b32 s23, s18, 0x60
	s_add_i32 m0, s43, 0x18000
	v_lshl_add_u64 v[2:3], v[2:3], 0, s[88:89]
	s_lshl_b32 s22, s5, 13
	s_lshl_b32 s24, s23, 7
	s_waitcnt vmcnt(2)
	s_barrier
	global_load_lds_dwordx4 v[2:3], off
	s_add_i32 m0, s43, 0x1a000
	s_add_u32 s28, s0, 0x6a200080
	v_mov_b32_e32 v173, v163
	v_lshl_add_u64 v[2:3], v[4:5], 0, s[88:89]
	s_addc_u32 s29, s1, 0
	s_add_i32 s49, s43, 0x8000
	s_add_i32 s50, s43, 0xa000
	v_mov_b32_e32 v175, v163
	global_load_lds_dwordx4 v[2:3], off
	v_lshl_add_u64 v[2:3], s[28:29], 0, v[172:173]
	s_mov_b32 m0, s49
	s_add_u32 s18, s8, 0x20080
	global_load_lds_dwordx4 v[2:3], off
	v_lshl_add_u64 v[2:3], s[28:29], 0, v[174:175]
	s_mov_b32 m0, s50
	s_addc_u32 s19, s9, 0
	global_load_lds_dwordx4 v[2:3], off
	s_add_i32 m0, s43, 0x1c000
	v_lshl_add_u64 v[2:3], s[18:19], 0, v[168:169]
	global_load_lds_dwordx4 v[2:3], off
	v_lshl_add_u64 v[2:3], s[18:19], 0, v[170:171]
	s_add_i32 m0, s43, 0x1e000
	s_cmpk_lt_u32 s4, 0x100
	global_load_lds_dwordx4 v[2:3], off
	v_lshrrev_b32_e32 v3, 1, v6
	v_and_b32_e32 v2, 15, v6
	v_and_b32_e32 v3, 24, v3
	v_lshl_or_b32 v173, s5, 6, v2
	v_lshlrev_b32_e32 v4, 1, v3
	v_lshl_or_b32 v2, v2, 6, v4
	v_lshlrev_b32_e32 v4, 2, v173
	v_and_b32_e32 v5, 32, v4
	v_lshlrev_b32_e32 v6, 2, v6
	s_waitcnt vmcnt(6)
	v_bitop3_b32 v5, v2, s22, v5 bitop3:0xde
	v_and_b32_e32 v6, 32, v6
	v_or_b32_e32 v195, 16, v173
	v_or_b32_e32 v252, 32, v173
	v_or_b32_e32 v198, 48, v173
	v_add_u32_e32 v164, 0x80, v173
	v_add_u32_e32 v165, 0x90, v173
	v_add_u32_e32 v208, 0xa0, v173
	v_add_u32_e32 v209, 0xb0, v173
	v_bitop3_b32 v175, v2, s24, v6 bitop3:0xde
	s_cselect_b64 s[30:31], -1, 0
	v_add_u32_e32 v210, s70, v4
	s_add_i32 s51, s16, -1
	v_or_b32_e32 v211, s23, v3
	v_lshl_add_u32 v212, v195, 2, s70
	v_lshl_add_u32 v213, v252, 2, s70
	v_lshl_add_u32 v214, v198, 2, s70
	v_lshl_add_u32 v215, v164, 2, s70
	v_lshl_add_u32 v216, v165, 2, s70
	v_lshl_add_u32 v217, v208, 2, s70
	v_lshl_add_u32 v218, v209, 2, s70
	s_mov_b32 s63, 0
	v_add_u32_e32 v219, 0, v5
	s_mov_b32 s61, 0
	s_barrier
	v_mov_b32_e32 v251, 0x76767676
	v_mov_b32_e32 v196, 0x79797979
	s_branch .LBB0_1218

; #define PG8_STAGE(bufoff, gbase, voff) do { _Pragma("unroll") for (int _i = 0; _i < 2; ++_i) \
;         __builtin_amdgcn_global_load_lds((const unsigned*)((const char*)(gbase) + (voff)[_i]), (PG8_LAS unsigned*)(lds + (bufoff) + ldsw + _i * 8192), 16, 0, 0); } while (0)
; #define PG8_STAGE_A(bufoff, gbase, h, nx) do { if constexpr (Sched::GATHER) { unsigned _v[2]; _Pragma("unroll") for (int _i = 0; _i < 2; ++_i) _v[_i] = (nx) ? vAn[h][_i] : vA[h][_i]; PG8_STAGE(bufoff, gbase, _v); } \
;         else { PG8_STAGE(bufoff, (gbase) + (h) * hstep, voffA); } } while (0)
; #define PG8_LDA(dst, b, h) do { _Pragma("unroll") for (int m = 0; m < 4; ++m) _Pragma("unroll") for (int k = 0; k < 2; ++k) dst[m][k] = *(const PG8_LAS bf16x8*)(lds + PG8_SA(b, h) + aoff + m * 2048 + k * 1024); } while (0)
; #define PG8_LDB(dst, b, h) do { _Pragma("unroll") for (int n = 0; n < 2; ++n) _Pragma("unroll") for (int k = 0; k < 2; ++k) dst[n][k] = *(const PG8_LAS bf16x8*)(lds + PG8_SB(b, h) + boff + n * 2048 + k * 1024); } while (0)
; #define PG8_WAIT_V(n) asm volatile("s_waitcnt vmcnt(" #n ")" ::: "memory")
; #define PG8_WAIT_L(n) asm volatile("s_waitcnt lgkmcnt(" #n ")" ::: "memory")
; #define PG8_BAR __builtin_amdgcn_s_barrier()
; #define PG8_SCHED __builtin_amdgcn_sched_barrier(0)
; template <class Epi, class Sched, bool ALIGN_EPI = false, bool SP2 = false, bool FP8 = false>
; __device__ __forceinline__ void gemm_phase(PG8_LAS unsigned char* lds, const Gemm g, const Sched& S, const Epi& E) {
;     ...
;             PG8_LDB(B0, 0, 0); PG8_LDB(B1, 0, 1); PG8_SCHED; PG8_LDA(At, 0, 0); PG8_STAGE_A(PG8_SA(1, 1), a1, 1, false);
;             PG8_WAIT_V(8); PG8_WAIT_L(0); PG8_BAR; PG8_MMA(0, 0, At, B0); PG8_MMA(0, 1, At, B1); PG8_BAR; PG8_SCHED;
;             PG8_LDA(At, 0, 1); PG8_STAGE(PG8_SB(0, 0), b2, voffB); PG8_STAGE(PG8_SB(0, 1), b2 + hstep, voffB); PG8_STAGE_A(PG8_SA(0, 0), a2, 0, last);
;             PG8_WAIT_V(8); PG8_WAIT_L(0); PG8_BAR; PG8_MMA(1, 0, At, B0); PG8_MMA(1, 1, At, B1); PG8_BAR; PG8_SCHED;
.LBB0_1223:
	s_add_u32 s8, s0, s44
	s_addc_u32 s9, s1, s45
	s_add_u32 s18, s8, 0x6a200100
	s_addc_u32 s19, s9, 0
	s_add_u32 s23, s39, s44
	s_addc_u32 s24, s64, s45
	s_add_i32 s22, 0, 0x10000
	s_cmpk_eq_i32 s44, 0x300
	s_cselect_b64 vcc, -1, 0
	s_and_b64 s[8:9], vcc, exec
	s_cselect_b32 s19, s7, s19
	s_cselect_b32 s18, s6, s18
	s_cselect_b32 s9, s4, s24
	s_cselect_b32 s8, s5, s23
	s_add_i32 s23, 0, 0x14000
	v_add_u32_e32 v2, s22, v175
	v_add_u32_e32 v6, s23, v175
	ds_read_b128 v[26:29], v2
	ds_read_b128 v[30:33], v2 offset:1024
	ds_read_b128 v[18:21], v2 offset:2048
	ds_read_b128 v[22:25], v2 offset:3072
	ds_read_b128 v[10:13], v6
	ds_read_b128 v[14:17], v6 offset:1024
	ds_read_b128 v[2:5], v6 offset:2048
	ds_read_b128 v[6:9], v6 offset:3072
	v_lshl_add_u64 v[200:201], v[182:183], 0, s[44:45]
	s_add_i32 m0, s43, 0xc000
	ds_read_b128 v[184:187], v219
	ds_read_b128 v[188:191], v219 offset:1024
	ds_read_b128 v[224:227], v219 offset:2048
	ds_read_b128 v[228:231], v219 offset:3072
	ds_read_b128 v[232:235], v219 offset:4096
	ds_read_b128 v[236:239], v219 offset:5120
	ds_read_b128 v[240:243], v219 offset:6144
	ds_read_b128 v[244:247], v219 offset:7168
	global_load_lds_dwordx4 v[200:201], off
	v_lshl_add_u64 v[200:201], v[180:181], 0, s[44:45]
	s_add_i32 m0, s43, 0xe000
	s_nop 0
	global_load_lds_dwordx4 v[200:201], off
	s_waitcnt vmcnt(8)
	s_waitcnt lgkmcnt(0)
	s_barrier
	s_setprio 1
	s_waitcnt lgkmcnt(0)
	v_mfma_scale_f32_16x16x128_f8f6f4 v[158:161], v[26:33], v[184:191], v[158:161], v251, v199 op_sel_hi:[0,0,0]
	v_mfma_scale_f32_16x16x128_f8f6f4 v[150:153], v[18:25], v[184:191], v[150:153], v251, v199 op_sel_hi:[0,0,0]
	v_mfma_scale_f32_16x16x128_f8f6f4 v[142:145], v[26:33], v[224:231], v[142:145], v251, v199 op_sel_hi:[0,0,0]
	v_mfma_scale_f32_16x16x128_f8f6f4 v[134:137], v[18:25], v[224:231], v[134:137], v251, v199 op_sel_hi:[0,0,0]
	v_mfma_scale_f32_16x16x128_f8f6f4 v[126:129], v[26:33], v[232:239], v[126:129], v251, v199 op_sel_hi:[0,0,0]
	v_mfma_scale_f32_16x16x128_f8f6f4 v[118:121], v[18:25], v[232:239], v[118:121], v251, v199 op_sel_hi:[0,0,0]
	v_mfma_scale_f32_16x16x128_f8f6f4 v[110:113], v[26:33], v[240:247], v[110:113], v251, v199 op_sel_hi:[0,0,0]
	v_mfma_scale_f32_16x16x128_f8f6f4 v[102:105], v[18:25], v[240:247], v[102:105], v251, v199 op_sel_hi:[0,0,0]
	s_setprio 0
	s_setprio 1
	v_mfma_scale_f32_16x16x128_f8f6f4 v[154:157], v[10:17], v[184:191], v[154:157], v196, v199 op_sel_hi:[0,0,0]
	v_mfma_scale_f32_16x16x128_f8f6f4 v[146:149], v[2:9], v[184:191], v[146:149], v196, v199 op_sel_hi:[0,0,0]
	v_mfma_scale_f32_16x16x128_f8f6f4 v[138:141], v[10:17], v[224:231], v[138:141], v196, v199 op_sel_hi:[0,0,0]
	v_mfma_scale_f32_16x16x128_f8f6f4 v[130:133], v[2:9], v[224:231], v[130:133], v196, v199 op_sel_hi:[0,0,0]
	v_mfma_scale_f32_16x16x128_f8f6f4 v[122:125], v[10:17], v[232:239], v[122:125], v196, v199 op_sel_hi:[0,0,0]
	v_mfma_scale_f32_16x16x128_f8f6f4 v[114:117], v[2:9], v[232:239], v[114:117], v196, v199 op_sel_hi:[0,0,0]
	v_mfma_scale_f32_16x16x128_f8f6f4 v[106:109], v[10:17], v[240:247], v[106:109], v196, v199 op_sel_hi:[0,0,0]
	v_mfma_scale_f32_16x16x128_f8f6f4 v[98:101], v[2:9], v[240:247], v[98:101], v196, v199 op_sel_hi:[0,0,0]
	s_setprio 0
	s_barrier
	s_add_i32 s22, s22, s34
	v_lshl_add_u64 v[184:185], s[8:9], 0, v[168:169]
	s_mov_b32 m0, s22
	ds_read_b128 v[224:227], v219 offset:16384
	ds_read_b128 v[228:231], v219 offset:17408
	ds_read_b128 v[232:235], v219 offset:18432
	ds_read_b128 v[236:239], v219 offset:19456
	ds_read_b128 v[240:243], v219 offset:20480
	ds_read_b128 v[244:247], v219 offset:21504
	ds_read_b128 v[200:203], v219 offset:22528
	ds_read_b128 v[204:207], v219 offset:23552
	global_load_lds_dwordx4 v[184:185], off
	s_add_i32 m0, s22, 0x2000
	s_add_u32 s24, s8, 0x20000
	v_lshl_add_u64 v[186:187], s[8:9], 0, v[170:171]
	s_addc_u32 s25, s9, 0
	s_add_i32 s22, s23, s34
	global_load_lds_dwordx4 v[186:187], off
	v_lshl_add_u64 v[188:189], s[24:25], 0, v[168:169]
	s_mov_b32 m0, s22
	v_cndmask_b32_e32 v162, v172, v222, vcc
	global_load_lds_dwordx4 v[188:189], off
	v_lshl_add_u64 v[188:189], s[24:25], 0, v[170:171]
	s_add_i32 m0, s22, 0x2000
	v_lshl_add_u64 v[190:191], s[18:19], 0, v[162:163]
	global_load_lds_dwordx4 v[188:189], off
	s_mov_b32 m0, s43
	v_cndmask_b32_e32 v188, v174, v220, vcc
	global_load_lds_dwordx4 v162, s[18:19]
	s_mov_b32 m0, s46
	v_mov_b32_e32 v189, v163
	global_load_lds_dwordx4 v188, s[18:19]
	s_waitcnt vmcnt(8)
	s_waitcnt lgkmcnt(0)
	v_lshl_add_u64 v[188:189], s[18:19], 0, v[188:189]
	s_barrier
	s_setprio 1
	s_waitcnt lgkmcnt(0)
	v_mfma_scale_f32_16x16x128_f8f6f4 v[94:97], v[26:33], v[224:231], v[94:97], v251, v199 op_sel_hi:[0,0,0]
	v_mfma_scale_f32_16x16x128_f8f6f4 v[86:89], v[18:25], v[224:231], v[86:89], v251, v199 op_sel_hi:[0,0,0]
	v_mfma_scale_f32_16x16x128_f8f6f4 v[74:77], v[26:33], v[232:239], v[74:77], v251, v199 op_sel_hi:[0,0,0]
	v_mfma_scale_f32_16x16x128_f8f6f4 v[66:69], v[18:25], v[232:239], v[66:69], v251, v199 op_sel_hi:[0,0,0]
	v_mfma_scale_f32_16x16x128_f8f6f4 v[58:61], v[26:33], v[240:247], v[58:61], v251, v199 op_sel_hi:[0,0,0]
	v_mfma_scale_f32_16x16x128_f8f6f4 v[50:53], v[18:25], v[240:247], v[50:53], v251, v199 op_sel_hi:[0,0,0]
	v_mfma_scale_f32_16x16x128_f8f6f4 v[42:45], v[26:33], v[200:207], v[42:45], v251, v199 op_sel_hi:[0,0,0]
	v_mfma_scale_f32_16x16x128_f8f6f4 v[34:37], v[18:25], v[200:207], v[34:37], v251, v199 op_sel_hi:[0,0,0]
	s_setprio 0
	s_setprio 1
	v_mfma_scale_f32_16x16x128_f8f6f4 v[90:93], v[10:17], v[224:231], v[90:93], v196, v199 op_sel_hi:[0,0,0]
	v_mfma_scale_f32_16x16x128_f8f6f4 v[82:85], v[2:9], v[224:231], v[82:85], v196, v199 op_sel_hi:[0,0,0]
	v_mfma_scale_f32_16x16x128_f8f6f4 v[78:81], v[10:17], v[232:239], v[78:81], v196, v199 op_sel_hi:[0,0,0]
	v_mfma_scale_f32_16x16x128_f8f6f4 v[70:73], v[2:9], v[232:239], v[70:73], v196, v199 op_sel_hi:[0,0,0]
	v_mfma_scale_f32_16x16x128_f8f6f4 v[62:65], v[10:17], v[240:247], v[62:65], v196, v199 op_sel_hi:[0,0,0]
	v_mfma_scale_f32_16x16x128_f8f6f4 v[54:57], v[2:9], v[240:247], v[54:57], v196, v199 op_sel_hi:[0,0,0]
	v_mfma_scale_f32_16x16x128_f8f6f4 v[46:49], v[10:17], v[200:207], v[46:49], v196, v199 op_sel_hi:[0,0,0]
	v_mfma_scale_f32_16x16x128_f8f6f4 v[38:41], v[2:9], v[200:207], v[38:41], v196, v199 op_sel_hi:[0,0,0]
	s_setprio 0
	s_barrier
; #define PG8_STAGE(bufoff, gbase, voff) do { _Pragma("unroll") for (int _i = 0; _i < 2; ++_i) \
;         __builtin_amdgcn_global_load_lds((const unsigned*)((const char*)(gbase) + (voff)[_i]), (PG8_LAS unsigned*)(lds + (bufoff) + ldsw + _i * 8192), 16, 0, 0); } while (0)
; #define PG8_STAGE_A(bufoff, gbase, h, nx) do { if constexpr (Sched::GATHER) { unsigned _v[2]; _Pragma("unroll") for (int _i = 0; _i < 2; ++_i) _v[_i] = (nx) ? vAn[h][_i] : vA[h][_i]; PG8_STAGE(bufoff, gbase, _v); } \
;         else { PG8_STAGE(bufoff, (gbase) + (h) * hstep, voffA); } } while (0)
; #define PG8_LDA(dst, b, h) do { _Pragma("unroll") for (int m = 0; m < 4; ++m) _Pragma("unroll") for (int k = 0; k < 2; ++k) dst[m][k] = *(const PG8_LAS bf16x8*)(lds + PG8_SA(b, h) + aoff + m * 2048 + k * 1024); } while (0)
; #define PG8_LDB(dst, b, h) do { _Pragma("unroll") for (int n = 0; n < 2; ++n) _Pragma("unroll") for (int k = 0; k < 2; ++k) dst[n][k] = *(const PG8_LAS bf16x8*)(lds + PG8_SB(b, h) + boff + n * 2048 + k * 1024); } while (0)
; #define PG8_WAIT_V(n) asm volatile("s_waitcnt vmcnt(" #n ")" ::: "memory")
; #define PG8_WAIT_L(n) asm volatile("s_waitcnt lgkmcnt(" #n ")" ::: "memory")
; #define PG8_BAR __builtin_amdgcn_s_barrier()
; #define PG8_SCHED __builtin_amdgcn_sched_barrier(0)
; template <class Epi, class Sched, bool ALIGN_EPI = false, bool SP2 = false, bool FP8 = false>
; __device__ __forceinline__ void gemm_phase(PG8_LAS unsigned char* lds, const Gemm g, const Sched& S, const Epi& E) {
;     ...
; #pragma unroll 1
;         for (int t = 0; t < nt; t += 2) {
;     ...
;             PG8_LDB(B0, 1, 0); PG8_LDB(B1, 1, 1); PG8_SCHED; PG8_LDA(At, 1, 0); PG8_STAGE_A(PG8_SA(0, 1), a2, 1, last);
;             PG8_WAIT_V(8); PG8_WAIT_L(0); PG8_BAR; PG8_MMA(0, 0, At, B0); PG8_MMA(0, 1, At, B1); PG8_BAR; PG8_SCHED;
;             PG8_LDA(At, 1, 1); PG8_STAGE(PG8_SB(1, 0), b3, voffB); PG8_STAGE(PG8_SB(1, 1), b3 + hstep, voffB); PG8_STAGE_A(PG8_SA(1, 0), a3, 0, last);
;             PG8_WAIT_V(8); PG8_WAIT_L(0); PG8_BAR; PG8_MMA(1, 0, At, B0); PG8_MMA(1, 1, At, B1); PG8_BAR; PG8_SCHED;
	s_add_i32 s22, 0, 0x18000
	s_add_i32 s23, 0, 0x1c000
	v_add_u32_e32 v14, s22, v175
	v_add_u32_e32 v30, s23, v175
	ds_read_b128 v[2:5], v14
	ds_read_b128 v[6:9], v14 offset:1024
	ds_read_b128 v[10:13], v14 offset:2048
	ds_read_b128 v[14:17], v14 offset:3072
	ds_read_b128 v[18:21], v30
	ds_read_b128 v[22:25], v30 offset:1024
	ds_read_b128 v[26:29], v30 offset:2048
	ds_read_b128 v[30:33], v30 offset:3072
	s_mov_b32 m0, s47
	v_cndmask_b32_e32 v162, v176, v221, vcc
	ds_read_b128 v[200:203], v219 offset:32768
	ds_read_b128 v[204:207], v219 offset:33792
	ds_read_b128 v[224:227], v219 offset:34816
	ds_read_b128 v[228:231], v219 offset:35840
	ds_read_b128 v[232:235], v219 offset:36864
	ds_read_b128 v[236:239], v219 offset:37888
	ds_read_b128 v[240:243], v219 offset:38912
	ds_read_b128 v[244:247], v219 offset:39936
	v_cndmask_b32_e32 v177, v178, v223, vcc
	global_load_lds_dwordx4 v162, s[18:19]
	s_mov_b32 m0, s48
	s_nop 0
	global_load_lds_dwordx4 v177, s[18:19]
	s_waitcnt vmcnt(8)
	s_waitcnt lgkmcnt(0)
	s_barrier
	s_setprio 1
	s_waitcnt lgkmcnt(0)
	v_mfma_scale_f32_16x16x128_f8f6f4 v[158:161], v[2:9], v[200:207], v[158:161], v251, v199 op_sel_hi:[0,0,0]
	v_mfma_scale_f32_16x16x128_f8f6f4 v[150:153], v[10:17], v[200:207], v[150:153], v251, v199 op_sel_hi:[0,0,0]
	v_mfma_scale_f32_16x16x128_f8f6f4 v[142:145], v[2:9], v[224:231], v[142:145], v251, v199 op_sel_hi:[0,0,0]
	v_mfma_scale_f32_16x16x128_f8f6f4 v[134:137], v[10:17], v[224:231], v[134:137], v251, v199 op_sel_hi:[0,0,0]
	v_mfma_scale_f32_16x16x128_f8f6f4 v[126:129], v[2:9], v[232:239], v[126:129], v251, v199 op_sel_hi:[0,0,0]
	v_mfma_scale_f32_16x16x128_f8f6f4 v[118:121], v[10:17], v[232:239], v[118:121], v251, v199 op_sel_hi:[0,0,0]
	v_mfma_scale_f32_16x16x128_f8f6f4 v[110:113], v[2:9], v[240:247], v[110:113], v251, v199 op_sel_hi:[0,0,0]
	v_mfma_scale_f32_16x16x128_f8f6f4 v[102:105], v[10:17], v[240:247], v[102:105], v251, v199 op_sel_hi:[0,0,0]
	s_setprio 0
	s_setprio 1
	v_mfma_scale_f32_16x16x128_f8f6f4 v[154:157], v[18:25], v[200:207], v[154:157], v196, v199 op_sel_hi:[0,0,0]
	v_mfma_scale_f32_16x16x128_f8f6f4 v[146:149], v[26:33], v[200:207], v[146:149], v196, v199 op_sel_hi:[0,0,0]
	v_mfma_scale_f32_16x16x128_f8f6f4 v[138:141], v[18:25], v[224:231], v[138:141], v196, v199 op_sel_hi:[0,0,0]
	v_mfma_scale_f32_16x16x128_f8f6f4 v[130:133], v[26:33], v[224:231], v[130:133], v196, v199 op_sel_hi:[0,0,0]
	v_mfma_scale_f32_16x16x128_f8f6f4 v[122:125], v[18:25], v[232:239], v[122:125], v196, v199 op_sel_hi:[0,0,0]
	v_mfma_scale_f32_16x16x128_f8f6f4 v[114:117], v[26:33], v[232:239], v[114:117], v196, v199 op_sel_hi:[0,0,0]
	v_mfma_scale_f32_16x16x128_f8f6f4 v[106:109], v[18:25], v[240:247], v[106:109], v196, v199 op_sel_hi:[0,0,0]
	v_mfma_scale_f32_16x16x128_f8f6f4 v[98:101], v[26:33], v[240:247], v[98:101], v196, v199 op_sel_hi:[0,0,0]
	s_setprio 0
	s_barrier
	s_add_i32 s18, s22, s34
	v_lshl_add_u64 v[184:185], v[184:185], 0, s[88:89]
	s_mov_b32 m0, s18
	ds_read_b128 v[200:203], v219 offset:49152
	ds_read_b128 v[204:207], v219 offset:50176
	ds_read_b128 v[224:227], v219 offset:51200
	ds_read_b128 v[228:231], v219 offset:52224
	ds_read_b128 v[232:235], v219 offset:53248
	ds_read_b128 v[236:239], v219 offset:54272
	ds_read_b128 v[240:243], v219 offset:55296
	ds_read_b128 v[244:247], v219 offset:56320
	global_load_lds_dwordx4 v[184:185], off
	s_add_i32 m0, s18, 0x2000
	s_add_u32 s8, s8, 0x20080
	v_lshl_add_u64 v[184:185], v[186:187], 0, s[88:89]
	s_addc_u32 s9, s9, 0
	s_add_i32 s18, s23, s34
	global_load_lds_dwordx4 v[184:185], off
	v_lshl_add_u64 v[184:185], s[8:9], 0, v[168:169]
	s_mov_b32 m0, s18
	s_nop 0
	global_load_lds_dwordx4 v[184:185], off
	v_lshl_add_u64 v[184:185], s[8:9], 0, v[170:171]
	s_add_i32 m0, s18, 0x2000
	s_nop 0
	global_load_lds_dwordx4 v[184:185], off
	v_lshl_add_u64 v[184:185], v[190:191], 0, s[88:89]
	s_mov_b32 m0, s49
	s_nop 0
	global_load_lds_dwordx4 v[184:185], off
	v_lshl_add_u64 v[184:185], v[188:189], 0, s[88:89]
	s_mov_b32 m0, s50
	s_nop 0
	global_load_lds_dwordx4 v[184:185], off
	s_waitcnt vmcnt(8)
	s_waitcnt lgkmcnt(0)
	s_barrier
	s_setprio 1
	s_waitcnt lgkmcnt(0)
	v_mfma_scale_f32_16x16x128_f8f6f4 v[94:97], v[2:9], v[200:207], v[94:97], v251, v199 op_sel_hi:[0,0,0]
	v_mfma_scale_f32_16x16x128_f8f6f4 v[86:89], v[10:17], v[200:207], v[86:89], v251, v199 op_sel_hi:[0,0,0]
	v_mfma_scale_f32_16x16x128_f8f6f4 v[74:77], v[2:9], v[224:231], v[74:77], v251, v199 op_sel_hi:[0,0,0]
	v_mfma_scale_f32_16x16x128_f8f6f4 v[66:69], v[10:17], v[224:231], v[66:69], v251, v199 op_sel_hi:[0,0,0]
	v_mfma_scale_f32_16x16x128_f8f6f4 v[58:61], v[2:9], v[232:239], v[58:61], v251, v199 op_sel_hi:[0,0,0]
	v_mfma_scale_f32_16x16x128_f8f6f4 v[50:53], v[10:17], v[232:239], v[50:53], v251, v199 op_sel_hi:[0,0,0]
	v_mfma_scale_f32_16x16x128_f8f6f4 v[42:45], v[2:9], v[240:247], v[42:45], v251, v199 op_sel_hi:[0,0,0]
	v_mfma_scale_f32_16x16x128_f8f6f4 v[34:37], v[10:17], v[240:247], v[34:37], v251, v199 op_sel_hi:[0,0,0]
	s_setprio 0
	s_setprio 1
	v_mfma_scale_f32_16x16x128_f8f6f4 v[90:93], v[18:25], v[200:207], v[90:93], v196, v199 op_sel_hi:[0,0,0]
	v_mfma_scale_f32_16x16x128_f8f6f4 v[82:85], v[26:33], v[200:207], v[82:85], v196, v199 op_sel_hi:[0,0,0]
	v_mfma_scale_f32_16x16x128_f8f6f4 v[78:81], v[18:25], v[224:231], v[78:81], v196, v199 op_sel_hi:[0,0,0]
	v_mfma_scale_f32_16x16x128_f8f6f4 v[70:73], v[26:33], v[224:231], v[70:73], v196, v199 op_sel_hi:[0,0,0]
	v_mfma_scale_f32_16x16x128_f8f6f4 v[62:65], v[18:25], v[232:239], v[62:65], v196, v199 op_sel_hi:[0,0,0]
	v_mfma_scale_f32_16x16x128_f8f6f4 v[54:57], v[26:33], v[232:239], v[54:57], v196, v199 op_sel_hi:[0,0,0]
	v_mfma_scale_f32_16x16x128_f8f6f4 v[46:49], v[18:25], v[240:247], v[46:49], v196, v199 op_sel_hi:[0,0,0]
	v_mfma_scale_f32_16x16x128_f8f6f4 v[38:41], v[26:33], v[240:247], v[38:41], v196, v199 op_sel_hi:[0,0,0]
	s_setprio 0
	s_barrier
	s_add_i32 s65, s65, 2
	s_add_u32 s44, s44, 0x100
	s_addc_u32 s45, s45, 0
	s_cmp_gt_u32 s65, 5
	s_cbranch_scc0 .LBB0_1223
	s_and_b64 vcc, exec, s[30:31]
	s_cbranch_vccz .LBB0_1226
	s_barrier
; __device__ __forceinline__ float siluf_(float x) { return x * __builtin_amdgcn_rcpf(1.f + __expf(-x)); }
;     __device__ __forceinline__ void operator()(const f32x4 (&acc)[2][2][4][2], const Unit& u, int wr, int wc, int fr, int fq) const {
;     ...
;             for (int m = 0; m < 4; ++m) { const int r = r0 + ai * 128 + m * 16;
;                 if (r < u.aux1) { const int pid = list[u.aux0 + r]; float o[8];
; #pragma unroll
;                     for (int n = 0; n < 2; ++n)
; #pragma unroll
;                         for (int i = 0; i < 4; ++i) o[n * 4 + i] = siluf_(acc[ai][0][m][n][i] * sc) * (acc[ai][1][m][n][i] * sc);
;                     v2u w; w.x = (unsigned)__builtin_amdgcn_cvt_pk_fp8_f32(o[2] * SA8, o[3] * SA8, __builtin_amdgcn_cvt_pk_fp8_f32(o[0] * SA8, o[1] * SA8, 0, false), true);
;                     w.y = (unsigned)__builtin_amdgcn_cvt_pk_fp8_f32(o[6] * SA8, o[7] * SA8, __builtin_amdgcn_cvt_pk_fp8_f32(o[4] * SA8, o[5] * SA8, 0, false), true);
;                     *(v2u*)(Act + (size_t)pid * 256 + col0) = w; } }
.LBB0_1226:
	s_lshl_b32 s4, s42, 7
	s_and_b32 s4, s4, 0x80
	v_or_b32_e32 v162, s4, v211
	v_cmp_gt_i32_e32 vcc, s62, v173
	s_and_saveexec_b64 s[8:9], vcc
	s_cbranch_execz .LBB0_1228
	v_lshl_add_u32 v2, s63, 2, v210
	ds_read_b32 v2, v2
	v_mul_f32_e32 v14, 0xbfb8aa3b, v158
	v_mul_f32_e32 v15, 0xbfb8aa3b, v159
	v_mul_f32_e32 v16, 0xbfb8aa3b, v160
	v_mul_f32_e32 v17, 0xbfb8aa3b, v161
	v_mul_f32_e32 v18, 0xbfb8aa3b, v150
	v_mul_f32_e32 v19, 0xbfb8aa3b, v151
	v_mul_f32_e32 v20, 0xbfb8aa3b, v152
	v_mul_f32_e32 v21, 0xbfb8aa3b, v153
	v_exp_f32_e32 v14, v14
	v_exp_f32_e32 v15, v15
	v_exp_f32_e32 v16, v16
	v_exp_f32_e32 v17, v17
	v_exp_f32_e32 v18, v18
	v_exp_f32_e32 v19, v19
	v_exp_f32_e32 v20, v20
	v_exp_f32_e32 v21, v21
	v_add_f32_e32 v14, 1.0, v14
	v_add_f32_e32 v15, 1.0, v15
	v_add_f32_e32 v16, 1.0, v16
	v_add_f32_e32 v17, 1.0, v17
	v_add_f32_e32 v18, 1.0, v18
	v_add_f32_e32 v19, 1.0, v19
	v_add_f32_e32 v20, 1.0, v20
	v_add_f32_e32 v21, 1.0, v21
	v_rcp_f32_e32 v14, v14
	v_rcp_f32_e32 v15, v15
	v_rcp_f32_e32 v16, v16
	v_rcp_f32_e32 v17, v17
	v_rcp_f32_e32 v18, v18
	v_rcp_f32_e32 v19, v19
	v_rcp_f32_e32 v20, v20
	v_rcp_f32_e32 v21, v21
	v_mul_f32_e32 v22, v158, v14
	v_mul_f32_e32 v23, v159, v15
	v_mul_f32_e32 v24, v160, v16
	v_mul_f32_e32 v25, v161, v17
	v_mul_f32_e32 v26, v150, v18
	v_mul_f32_e32 v27, v151, v19
	v_mul_f32_e32 v28, v152, v20
	v_mul_f32_e32 v29, v153, v21
	v_mul_f32_e32 v22, v22, v154
	v_mul_f32_e32 v23, v23, v155
	v_mul_f32_e32 v24, v24, v156
	v_mul_f32_e32 v25, v25, v157
	v_mul_f32_e32 v26, v26, v146
	v_mul_f32_e32 v27, v27, v147
	v_mul_f32_e32 v28, v28, v148
	v_mul_f32_e32 v29, v29, v149
	s_waitcnt lgkmcnt(0)
	v_ashrrev_i32_e32 v3, 31, v2
	v_lshlrev_b64 v[2:3], 8, v[2:3]
	v_lshl_add_u64 v[2:3], s[20:21], 0, v[2:3]
	v_lshl_add_u64 v[2:3], v[2:3], 0, v[162:163]
	v_mov_b32_e32 v4, v163
	v_mov_b32_e32 v5, v163
	v_cvt_pk_fp8_f32 v4, v22, v23
	v_cvt_pk_fp8_f32 v5, v26, v27
	v_cvt_pk_fp8_f32 v4, v24, v25 op_sel:[0,0,1]
	v_cvt_pk_fp8_f32 v5, v28, v29 op_sel:[0,0,1]
	s_nop 0
	global_store_dwordx2 v[2:3], v[4:5], off
.LBB0_1228:
	s_or_b64 exec, exec, s[8:9]
	v_cmp_gt_i32_e32 vcc, s62, v195
	s_and_saveexec_b64 s[8:9], vcc
	s_cbranch_execz .LBB0_1230
	v_lshl_add_u32 v2, s63, 2, v212
	ds_read_b32 v2, v2
	v_mul_f32_e32 v14, 0xbfb8aa3b, v142
	v_mul_f32_e32 v15, 0xbfb8aa3b, v143
	v_mul_f32_e32 v16, 0xbfb8aa3b, v144
	v_mul_f32_e32 v17, 0xbfb8aa3b, v145
	v_mul_f32_e32 v18, 0xbfb8aa3b, v134
	v_mul_f32_e32 v19, 0xbfb8aa3b, v135
	v_mul_f32_e32 v20, 0xbfb8aa3b, v136
	v_mul_f32_e32 v21, 0xbfb8aa3b, v137
	v_exp_f32_e32 v14, v14
	v_exp_f32_e32 v15, v15
	v_exp_f32_e32 v16, v16
	v_exp_f32_e32 v17, v17
	v_exp_f32_e32 v18, v18
	v_exp_f32_e32 v19, v19
	v_exp_f32_e32 v20, v20
	v_exp_f32_e32 v21, v21
	v_add_f32_e32 v14, 1.0, v14
	v_add_f32_e32 v15, 1.0, v15
	v_add_f32_e32 v16, 1.0, v16
	v_add_f32_e32 v17, 1.0, v17
	v_add_f32_e32 v18, 1.0, v18
	v_add_f32_e32 v19, 1.0, v19
	v_add_f32_e32 v20, 1.0, v20
	v_add_f32_e32 v21, 1.0, v21
	v_rcp_f32_e32 v14, v14
	v_rcp_f32_e32 v15, v15
	v_rcp_f32_e32 v16, v16
	v_rcp_f32_e32 v17, v17
	v_rcp_f32_e32 v18, v18
	v_rcp_f32_e32 v19, v19
	v_rcp_f32_e32 v20, v20
	v_rcp_f32_e32 v21, v21
	v_mul_f32_e32 v22, v142, v14
	v_mul_f32_e32 v23, v143, v15
	v_mul_f32_e32 v24, v144, v16
	v_mul_f32_e32 v25, v145, v17
	v_mul_f32_e32 v26, v134, v18
	v_mul_f32_e32 v27, v135, v19
	v_mul_f32_e32 v28, v136, v20
	v_mul_f32_e32 v29, v137, v21
	v_mul_f32_e32 v22, v22, v138
	v_mul_f32_e32 v23, v23, v139
	v_mul_f32_e32 v24, v24, v140
	v_mul_f32_e32 v25, v25, v141
	v_mul_f32_e32 v26, v26, v130
	v_mul_f32_e32 v27, v27, v131
	v_mul_f32_e32 v28, v28, v132
	v_mul_f32_e32 v29, v29, v133
	s_waitcnt lgkmcnt(0)
	v_ashrrev_i32_e32 v3, 31, v2
	v_lshlrev_b64 v[2:3], 8, v[2:3]
	v_lshl_add_u64 v[2:3], s[20:21], 0, v[2:3]
	v_lshl_add_u64 v[2:3], v[2:3], 0, v[162:163]
	v_mov_b32_e32 v4, v163
	v_mov_b32_e32 v5, v163
	v_cvt_pk_fp8_f32 v4, v22, v23
	v_cvt_pk_fp8_f32 v5, v26, v27
	v_cvt_pk_fp8_f32 v4, v24, v25 op_sel:[0,0,1]
	v_cvt_pk_fp8_f32 v5, v28, v29 op_sel:[0,0,1]
	s_nop 0
	global_store_dwordx2 v[2:3], v[4:5], off

; __device__ __forceinline__ float siluf_(float x) { return x * __builtin_amdgcn_rcpf(1.f + __expf(-x)); }
;     __device__ __forceinline__ void operator()(const f32x4 (&acc)[2][2][4][2], const Unit& u, int wr, int wc, int fr, int fq) const {
;     ...
;             for (int m = 0; m < 4; ++m) { const int r = r0 + ai * 128 + m * 16;
;                 if (r < u.aux1) { const int pid = list[u.aux0 + r]; float o[8];
; #pragma unroll
;                     for (int n = 0; n < 2; ++n)
; #pragma unroll
;                         for (int i = 0; i < 4; ++i) o[n * 4 + i] = siluf_(acc[ai][0][m][n][i] * sc) * (acc[ai][1][m][n][i] * sc);
;                     v2u w; w.x = (unsigned)__builtin_amdgcn_cvt_pk_fp8_f32(o[2] * SA8, o[3] * SA8, __builtin_amdgcn_cvt_pk_fp8_f32(o[0] * SA8, o[1] * SA8, 0, false), true);
;                     w.y = (unsigned)__builtin_amdgcn_cvt_pk_fp8_f32(o[6] * SA8, o[7] * SA8, __builtin_amdgcn_cvt_pk_fp8_f32(o[4] * SA8, o[5] * SA8, 0, false), true);
;                     *(v2u*)(Act + (size_t)pid * 256 + col0) = w; } }
.LBB0_1237:
	v_lshl_add_u32 v2, s63, 2, v213
	ds_read_b32 v2, v2
	v_mul_f32_e32 v14, 0xbfb8aa3b, v126
	v_mul_f32_e32 v15, 0xbfb8aa3b, v127
	v_mul_f32_e32 v16, 0xbfb8aa3b, v128
	v_mul_f32_e32 v17, 0xbfb8aa3b, v129
	v_mul_f32_e32 v18, 0xbfb8aa3b, v118
	v_mul_f32_e32 v19, 0xbfb8aa3b, v119
	v_mul_f32_e32 v20, 0xbfb8aa3b, v120
	v_mul_f32_e32 v21, 0xbfb8aa3b, v121
	v_exp_f32_e32 v14, v14
	v_exp_f32_e32 v15, v15
	v_exp_f32_e32 v16, v16
	v_exp_f32_e32 v17, v17
	v_exp_f32_e32 v18, v18
	v_exp_f32_e32 v19, v19
	v_exp_f32_e32 v20, v20
	v_exp_f32_e32 v21, v21
	v_add_f32_e32 v14, 1.0, v14
	v_add_f32_e32 v15, 1.0, v15
	v_add_f32_e32 v16, 1.0, v16
	v_add_f32_e32 v17, 1.0, v17
	v_add_f32_e32 v18, 1.0, v18
	v_add_f32_e32 v19, 1.0, v19
	v_add_f32_e32 v20, 1.0, v20
	v_add_f32_e32 v21, 1.0, v21
	v_rcp_f32_e32 v14, v14
	v_rcp_f32_e32 v15, v15
	v_rcp_f32_e32 v16, v16
	v_rcp_f32_e32 v17, v17
	v_rcp_f32_e32 v18, v18
	v_rcp_f32_e32 v19, v19
	v_rcp_f32_e32 v20, v20
	v_rcp_f32_e32 v21, v21
	v_mul_f32_e32 v22, v126, v14
	v_mul_f32_e32 v23, v127, v15
	v_mul_f32_e32 v24, v128, v16
	v_mul_f32_e32 v25, v129, v17
	v_mul_f32_e32 v26, v118, v18
	v_mul_f32_e32 v27, v119, v19
	v_mul_f32_e32 v28, v120, v20
	v_mul_f32_e32 v29, v121, v21
	v_mul_f32_e32 v22, v22, v122
	v_mul_f32_e32 v23, v23, v123
	v_mul_f32_e32 v24, v24, v124
	v_mul_f32_e32 v25, v25, v125
	v_mul_f32_e32 v26, v26, v114
	v_mul_f32_e32 v27, v27, v115
	v_mul_f32_e32 v28, v28, v116
	v_mul_f32_e32 v29, v29, v117
	s_waitcnt lgkmcnt(0)
	v_ashrrev_i32_e32 v3, 31, v2
	v_lshlrev_b64 v[2:3], 8, v[2:3]
	v_lshl_add_u64 v[2:3], s[20:21], 0, v[2:3]
	v_lshl_add_u64 v[2:3], v[2:3], 0, v[162:163]
	v_mov_b32_e32 v4, v163
	v_mov_b32_e32 v5, v163
	v_cvt_pk_fp8_f32 v4, v22, v23
	v_cvt_pk_fp8_f32 v5, v26, v27
	v_cvt_pk_fp8_f32 v4, v24, v25 op_sel:[0,0,1]
	v_cvt_pk_fp8_f32 v5, v28, v29 op_sel:[0,0,1]
	s_nop 0
	global_store_dwordx2 v[2:3], v[4:5], off
	s_or_b64 exec, exec, s[8:9]
	v_cmp_gt_i32_e32 vcc, s62, v198
	s_and_saveexec_b64 s[8:9], vcc
	s_cbranch_execz .LBB0_1232
.LBB0_1238:
	v_lshl_add_u32 v2, s63, 2, v214
	ds_read_b32 v2, v2
	v_mul_f32_e32 v14, 0xbfb8aa3b, v110
	v_mul_f32_e32 v15, 0xbfb8aa3b, v111
	v_mul_f32_e32 v16, 0xbfb8aa3b, v112
	v_mul_f32_e32 v17, 0xbfb8aa3b, v113
	v_mul_f32_e32 v18, 0xbfb8aa3b, v102
	v_mul_f32_e32 v19, 0xbfb8aa3b, v103
	v_mul_f32_e32 v20, 0xbfb8aa3b, v104
	v_mul_f32_e32 v21, 0xbfb8aa3b, v105
	v_exp_f32_e32 v14, v14
	v_exp_f32_e32 v15, v15
	v_exp_f32_e32 v16, v16
	v_exp_f32_e32 v17, v17
	v_exp_f32_e32 v18, v18
	v_exp_f32_e32 v19, v19
	v_exp_f32_e32 v20, v20
	v_exp_f32_e32 v21, v21
	v_add_f32_e32 v14, 1.0, v14
	v_add_f32_e32 v15, 1.0, v15
	v_add_f32_e32 v16, 1.0, v16
	v_add_f32_e32 v17, 1.0, v17
	v_add_f32_e32 v18, 1.0, v18
	v_add_f32_e32 v19, 1.0, v19
	v_add_f32_e32 v20, 1.0, v20
	v_add_f32_e32 v21, 1.0, v21
	v_rcp_f32_e32 v14, v14
	v_rcp_f32_e32 v15, v15
	v_rcp_f32_e32 v16, v16
	v_rcp_f32_e32 v17, v17
	v_rcp_f32_e32 v18, v18
	v_rcp_f32_e32 v19, v19
	v_rcp_f32_e32 v20, v20
	v_rcp_f32_e32 v21, v21
	v_mul_f32_e32 v22, v110, v14
	v_mul_f32_e32 v23, v111, v15
	v_mul_f32_e32 v24, v112, v16
	v_mul_f32_e32 v25, v113, v17
	v_mul_f32_e32 v26, v102, v18
	v_mul_f32_e32 v27, v103, v19
	v_mul_f32_e32 v28, v104, v20
	v_mul_f32_e32 v29, v105, v21
	v_mul_f32_e32 v22, v22, v106
	v_mul_f32_e32 v23, v23, v107
	v_mul_f32_e32 v24, v24, v108
	v_mul_f32_e32 v25, v25, v109
	v_mul_f32_e32 v26, v26, v98
	v_mul_f32_e32 v27, v27, v99
	v_mul_f32_e32 v28, v28, v100
	v_mul_f32_e32 v29, v29, v101
	s_waitcnt lgkmcnt(0)
	v_ashrrev_i32_e32 v3, 31, v2
	v_lshlrev_b64 v[2:3], 8, v[2:3]
	v_lshl_add_u64 v[2:3], s[20:21], 0, v[2:3]
	v_lshl_add_u64 v[2:3], v[2:3], 0, v[162:163]
	v_mov_b32_e32 v4, v163
	v_mov_b32_e32 v5, v163
	v_cvt_pk_fp8_f32 v4, v22, v23
	v_cvt_pk_fp8_f32 v5, v26, v27
	v_cvt_pk_fp8_f32 v4, v24, v25 op_sel:[0,0,1]
	v_cvt_pk_fp8_f32 v5, v28, v29 op_sel:[0,0,1]
	s_nop 0
	global_store_dwordx2 v[2:3], v[4:5], off
	s_or_b64 exec, exec, s[8:9]
	v_cmp_gt_i32_e32 vcc, s62, v164
	s_and_saveexec_b64 s[8:9], vcc
	s_cbranch_execz .LBB0_1233
.LBB0_1239:
	v_lshl_add_u32 v2, s63, 2, v215
	ds_read_b32 v2, v2
	v_mul_f32_e32 v14, 0xbfb8aa3b, v94
	v_mul_f32_e32 v15, 0xbfb8aa3b, v95
	v_mul_f32_e32 v16, 0xbfb8aa3b, v96
	v_mul_f32_e32 v17, 0xbfb8aa3b, v97
	v_mul_f32_e32 v18, 0xbfb8aa3b, v86
	v_mul_f32_e32 v19, 0xbfb8aa3b, v87
	v_mul_f32_e32 v20, 0xbfb8aa3b, v88
	v_mul_f32_e32 v21, 0xbfb8aa3b, v89
	v_exp_f32_e32 v14, v14
	v_exp_f32_e32 v15, v15
	v_exp_f32_e32 v16, v16
	v_exp_f32_e32 v17, v17
	v_exp_f32_e32 v18, v18
	v_exp_f32_e32 v19, v19
	v_exp_f32_e32 v20, v20
	v_exp_f32_e32 v21, v21
	v_add_f32_e32 v14, 1.0, v14
	v_add_f32_e32 v15, 1.0, v15
	v_add_f32_e32 v16, 1.0, v16
	v_add_f32_e32 v17, 1.0, v17
	v_add_f32_e32 v18, 1.0, v18
	v_add_f32_e32 v19, 1.0, v19
	v_add_f32_e32 v20, 1.0, v20
	v_add_f32_e32 v21, 1.0, v21
	v_rcp_f32_e32 v14, v14
	v_rcp_f32_e32 v15, v15
	v_rcp_f32_e32 v16, v16
	v_rcp_f32_e32 v17, v17
	v_rcp_f32_e32 v18, v18
	v_rcp_f32_e32 v19, v19
	v_rcp_f32_e32 v20, v20
	v_rcp_f32_e32 v21, v21
	v_mul_f32_e32 v22, v94, v14
	v_mul_f32_e32 v23, v95, v15
	v_mul_f32_e32 v24, v96, v16
	v_mul_f32_e32 v25, v97, v17
	v_mul_f32_e32 v26, v86, v18
	v_mul_f32_e32 v27, v87, v19
	v_mul_f32_e32 v28, v88, v20
	v_mul_f32_e32 v29, v89, v21
	v_mul_f32_e32 v22, v22, v90
	v_mul_f32_e32 v23, v23, v91
	v_mul_f32_e32 v24, v24, v92
	v_mul_f32_e32 v25, v25, v93
	v_mul_f32_e32 v26, v26, v82
	v_mul_f32_e32 v27, v27, v83
	v_mul_f32_e32 v28, v28, v84
	v_mul_f32_e32 v29, v29, v85
	s_waitcnt lgkmcnt(0)
	v_ashrrev_i32_e32 v3, 31, v2
	v_lshlrev_b64 v[2:3], 8, v[2:3]
	v_lshl_add_u64 v[2:3], s[20:21], 0, v[2:3]
	v_lshl_add_u64 v[2:3], v[2:3], 0, v[162:163]
	v_mov_b32_e32 v4, v163
	v_mov_b32_e32 v5, v163
	v_cvt_pk_fp8_f32 v4, v22, v23
	v_cvt_pk_fp8_f32 v5, v26, v27
	v_cvt_pk_fp8_f32 v4, v24, v25 op_sel:[0,0,1]
	v_cvt_pk_fp8_f32 v5, v28, v29 op_sel:[0,0,1]
	s_nop 0
	global_store_dwordx2 v[2:3], v[4:5], off
	s_or_b64 exec, exec, s[8:9]
	v_cmp_gt_i32_e32 vcc, s62, v165
	s_and_saveexec_b64 s[8:9], vcc
	s_cbranch_execz .LBB0_1234
; __device__ __forceinline__ float siluf_(float x) { return x * __builtin_amdgcn_rcpf(1.f + __expf(-x)); }
;     __device__ __forceinline__ void operator()(const f32x4 (&acc)[2][2][4][2], const Unit& u, int wr, int wc, int fr, int fq) const {
;         const int r0 = wr * 64 + fr, col0 = (u.pn & 1) * 128 + wc * 32 + 8 * fq;
;     ...
;             for (int m = 0; m < 4; ++m) { const int r = r0 + ai * 128 + m * 16;
;                 if (r < u.aux1) { const int pid = list[u.aux0 + r]; float o[8];
; #pragma unroll
;                     for (int n = 0; n < 2; ++n)
; #pragma unroll
;                         for (int i = 0; i < 4; ++i) o[n * 4 + i] = siluf_(acc[ai][0][m][n][i] * sc) * (acc[ai][1][m][n][i] * sc);
;                     v2u w; w.x = (unsigned)__builtin_amdgcn_cvt_pk_fp8_f32(o[2] * SA8, o[3] * SA8, __builtin_amdgcn_cvt_pk_fp8_f32(o[0] * SA8, o[1] * SA8, 0, false), true);
;                     w.y = (unsigned)__builtin_amdgcn_cvt_pk_fp8_f32(o[6] * SA8, o[7] * SA8, __builtin_amdgcn_cvt_pk_fp8_f32(o[4] * SA8, o[5] * SA8, 0, false), true);
;                     *(v2u*)(Act + (size_t)pid * 256 + col0) = w; } }
.LBB0_1240:
	v_lshl_add_u32 v2, s63, 2, v216
	ds_read_b32 v2, v2
	v_mul_f32_e32 v14, 0xbfb8aa3b, v74
	v_mul_f32_e32 v15, 0xbfb8aa3b, v75
	v_mul_f32_e32 v16, 0xbfb8aa3b, v76
	v_mul_f32_e32 v17, 0xbfb8aa3b, v77
	v_mul_f32_e32 v18, 0xbfb8aa3b, v66
	v_mul_f32_e32 v19, 0xbfb8aa3b, v67
	v_mul_f32_e32 v20, 0xbfb8aa3b, v68
	v_mul_f32_e32 v21, 0xbfb8aa3b, v69
	v_exp_f32_e32 v14, v14
	v_exp_f32_e32 v15, v15
	v_exp_f32_e32 v16, v16
	v_exp_f32_e32 v17, v17
	v_exp_f32_e32 v18, v18
	v_exp_f32_e32 v19, v19
	v_exp_f32_e32 v20, v20
	v_exp_f32_e32 v21, v21
	v_add_f32_e32 v14, 1.0, v14
	v_add_f32_e32 v15, 1.0, v15
	v_add_f32_e32 v16, 1.0, v16
	v_add_f32_e32 v17, 1.0, v17
	v_add_f32_e32 v18, 1.0, v18
	v_add_f32_e32 v19, 1.0, v19
	v_add_f32_e32 v20, 1.0, v20
	v_add_f32_e32 v21, 1.0, v21
	v_rcp_f32_e32 v14, v14
	v_rcp_f32_e32 v15, v15
	v_rcp_f32_e32 v16, v16
	v_rcp_f32_e32 v17, v17
	v_rcp_f32_e32 v18, v18
	v_rcp_f32_e32 v19, v19
	v_rcp_f32_e32 v20, v20
	v_rcp_f32_e32 v21, v21
	v_mul_f32_e32 v22, v74, v14
	v_mul_f32_e32 v23, v75, v15
	v_mul_f32_e32 v24, v76, v16
	v_mul_f32_e32 v25, v77, v17
	v_mul_f32_e32 v26, v66, v18
	v_mul_f32_e32 v27, v67, v19
	v_mul_f32_e32 v28, v68, v20
	v_mul_f32_e32 v29, v69, v21
	v_mul_f32_e32 v22, v22, v78
	v_mul_f32_e32 v23, v23, v79
	v_mul_f32_e32 v24, v24, v80
	v_mul_f32_e32 v25, v25, v81
	v_mul_f32_e32 v26, v26, v70
	v_mul_f32_e32 v27, v27, v71
	v_mul_f32_e32 v28, v28, v72
	v_mul_f32_e32 v29, v29, v73
	s_waitcnt lgkmcnt(0)
	v_ashrrev_i32_e32 v3, 31, v2
	v_lshlrev_b64 v[2:3], 8, v[2:3]
	v_lshl_add_u64 v[2:3], s[20:21], 0, v[2:3]
	v_lshl_add_u64 v[2:3], v[2:3], 0, v[162:163]
	v_mov_b32_e32 v4, v163
	v_mov_b32_e32 v5, v163
	v_cvt_pk_fp8_f32 v4, v22, v23
	v_cvt_pk_fp8_f32 v5, v26, v27
	v_cvt_pk_fp8_f32 v4, v24, v25 op_sel:[0,0,1]
	v_cvt_pk_fp8_f32 v5, v28, v29 op_sel:[0,0,1]
	s_nop 0
	global_store_dwordx2 v[2:3], v[4:5], off
	s_or_b64 exec, exec, s[8:9]
	v_cmp_gt_i32_e32 vcc, s62, v208
	s_and_saveexec_b64 s[8:9], vcc
	s_cbranch_execz .LBB0_1235
.LBB0_1241:
	v_lshl_add_u32 v2, s63, 2, v217
	ds_read_b32 v2, v2
	v_mul_f32_e32 v14, 0xbfb8aa3b, v58
	v_mul_f32_e32 v15, 0xbfb8aa3b, v59
	v_mul_f32_e32 v16, 0xbfb8aa3b, v60
	v_mul_f32_e32 v17, 0xbfb8aa3b, v61
	v_mul_f32_e32 v18, 0xbfb8aa3b, v50
	v_mul_f32_e32 v19, 0xbfb8aa3b, v51
	v_mul_f32_e32 v20, 0xbfb8aa3b, v52
	v_mul_f32_e32 v21, 0xbfb8aa3b, v53
	v_exp_f32_e32 v14, v14
	v_exp_f32_e32 v15, v15
	v_exp_f32_e32 v16, v16
	v_exp_f32_e32 v17, v17
	v_exp_f32_e32 v18, v18
	v_exp_f32_e32 v19, v19
	v_exp_f32_e32 v20, v20
	v_exp_f32_e32 v21, v21
	v_add_f32_e32 v14, 1.0, v14
	v_add_f32_e32 v15, 1.0, v15
	v_add_f32_e32 v16, 1.0, v16
	v_add_f32_e32 v17, 1.0, v17
	v_add_f32_e32 v18, 1.0, v18
	v_add_f32_e32 v19, 1.0, v19
	v_add_f32_e32 v20, 1.0, v20
	v_add_f32_e32 v21, 1.0, v21
	v_rcp_f32_e32 v14, v14
	v_rcp_f32_e32 v15, v15
	v_rcp_f32_e32 v16, v16
	v_rcp_f32_e32 v17, v17
	v_rcp_f32_e32 v18, v18
	v_rcp_f32_e32 v19, v19
	v_rcp_f32_e32 v20, v20
	v_rcp_f32_e32 v21, v21
	v_mul_f32_e32 v22, v58, v14
	v_mul_f32_e32 v23, v59, v15
	v_mul_f32_e32 v24, v60, v16
	v_mul_f32_e32 v25, v61, v17
	v_mul_f32_e32 v26, v50, v18
	v_mul_f32_e32 v27, v51, v19
	v_mul_f32_e32 v28, v52, v20
	v_mul_f32_e32 v29, v53, v21
	v_mul_f32_e32 v22, v22, v62
	v_mul_f32_e32 v23, v23, v63
	v_mul_f32_e32 v24, v24, v64
	v_mul_f32_e32 v25, v25, v65
	v_mul_f32_e32 v26, v26, v54
	v_mul_f32_e32 v27, v27, v55
	v_mul_f32_e32 v28, v28, v56
	v_mul_f32_e32 v29, v29, v57
	s_waitcnt lgkmcnt(0)
	v_ashrrev_i32_e32 v3, 31, v2
	v_lshlrev_b64 v[2:3], 8, v[2:3]
	v_lshl_add_u64 v[2:3], s[20:21], 0, v[2:3]
	v_lshl_add_u64 v[2:3], v[2:3], 0, v[162:163]
	v_mov_b32_e32 v4, v163
	v_mov_b32_e32 v5, v163
	v_cvt_pk_fp8_f32 v4, v22, v23
	v_cvt_pk_fp8_f32 v5, v26, v27
	v_cvt_pk_fp8_f32 v4, v24, v25 op_sel:[0,0,1]
	v_cvt_pk_fp8_f32 v5, v28, v29 op_sel:[0,0,1]
	s_nop 0
	global_store_dwordx2 v[2:3], v[4:5], off
	s_or_b64 exec, exec, s[8:9]
	v_cmp_gt_i32_e32 vcc, s62, v209
	s_and_saveexec_b64 s[8:9], vcc
	s_cbranch_execz .LBB0_1236
.LBB0_1242:
	v_lshl_add_u32 v2, s63, 2, v218
	ds_read_b32 v2, v2
	v_mul_f32_e32 v14, 0xbfb8aa3b, v42
	v_mul_f32_e32 v15, 0xbfb8aa3b, v43
	v_mul_f32_e32 v16, 0xbfb8aa3b, v44
	v_mul_f32_e32 v17, 0xbfb8aa3b, v45
	v_mul_f32_e32 v18, 0xbfb8aa3b, v34
	v_mul_f32_e32 v19, 0xbfb8aa3b, v35
	v_mul_f32_e32 v20, 0xbfb8aa3b, v36
	v_mul_f32_e32 v21, 0xbfb8aa3b, v37
	v_exp_f32_e32 v14, v14
	v_exp_f32_e32 v15, v15
	v_exp_f32_e32 v16, v16
	v_exp_f32_e32 v17, v17
	v_exp_f32_e32 v18, v18
	v_exp_f32_e32 v19, v19
	v_exp_f32_e32 v20, v20
	v_exp_f32_e32 v21, v21
	v_add_f32_e32 v14, 1.0, v14
	v_add_f32_e32 v15, 1.0, v15
	v_add_f32_e32 v16, 1.0, v16
	v_add_f32_e32 v17, 1.0, v17
	v_add_f32_e32 v18, 1.0, v18
	v_add_f32_e32 v19, 1.0, v19
	v_add_f32_e32 v20, 1.0, v20
	v_add_f32_e32 v21, 1.0, v21
	v_rcp_f32_e32 v14, v14
	v_rcp_f32_e32 v15, v15
	v_rcp_f32_e32 v16, v16
	v_rcp_f32_e32 v17, v17
	v_rcp_f32_e32 v18, v18
	v_rcp_f32_e32 v19, v19
	v_rcp_f32_e32 v20, v20
	v_rcp_f32_e32 v21, v21
	v_mul_f32_e32 v22, v42, v14
	v_mul_f32_e32 v23, v43, v15
	v_mul_f32_e32 v24, v44, v16
	v_mul_f32_e32 v25, v45, v17
	v_mul_f32_e32 v26, v34, v18
	v_mul_f32_e32 v27, v35, v19
	v_mul_f32_e32 v28, v36, v20
	v_mul_f32_e32 v29, v37, v21
	v_mul_f32_e32 v22, v22, v46
	v_mul_f32_e32 v23, v23, v47
	v_mul_f32_e32 v24, v24, v48
	v_mul_f32_e32 v25, v25, v49
	v_mul_f32_e32 v26, v26, v38
	v_mul_f32_e32 v27, v27, v39
	v_mul_f32_e32 v28, v28, v40
	v_mul_f32_e32 v29, v29, v41
	s_waitcnt lgkmcnt(0)
	v_ashrrev_i32_e32 v3, 31, v2
	v_lshlrev_b64 v[2:3], 8, v[2:3]
	v_lshl_add_u64 v[2:3], s[20:21], 0, v[2:3]
	v_lshl_add_u64 v[2:3], v[2:3], 0, v[162:163]
	v_mov_b32_e32 v4, v163
	v_mov_b32_e32 v5, v163
	v_cvt_pk_fp8_f32 v4, v22, v23
	v_cvt_pk_fp8_f32 v5, v26, v27
	v_cvt_pk_fp8_f32 v4, v24, v25 op_sel:[0,0,1]
	v_cvt_pk_fp8_f32 v5, v28, v29 op_sel:[0,0,1]
	s_nop 0
	global_store_dwordx2 v[2:3], v[4:5], off
	s_or_b64 exec, exec, s[8:9]
	s_cmp_eq_u32 s61, s51
	s_mov_b64 s[8:9], -1
	s_cbranch_scc1 .LBB0_1217

; #define SEAM(k) do { } while (0)
; #define SEAM(k) do { if ((k) + 1 < hi) xcd_barrier(bar); } while (0)
; #define PTRS() Ptrs P; load_ptrs(P); unsigned char* const ws = P.ws; (void)ws
; __global__ void __launch_bounds__(NTHR, 2) mk_fwd(Args args) {
;     ...
;     for (int layer = 0; layer < NL; ++layer) {
;         const int k0 = 2 + layer * 13;
;         if (EN(2) && IN(k0 + 0)) { PTRS(); if (layer == 0) phase_rowpass1<0>(P, lds, layer, 0, vcu, G); else phase_rowpass1<1>(P, lds, layer, 0, vcu, G); SEAM(k0 + 0); }
.LBB0_1315:
	v_mov_b32_e32 v196, 0x358637bd
	s_cmp_le_i32 s56, s4
	s_cselect_b64 s[0:1], -1, 0
	s_cmp_lt_i32 s4, s57
	s_cselect_b64 s[4:5], -1, 0
	s_and_b64 s[4:5], s[0:1], s[4:5]
	s_mov_b64 s[0:1], -1
	s_and_b64 vcc, exec, s[4:5]
	s_cbranch_vccnz .LBB0_1317
	s_add_i32 s4, s87, 13
	s_mov_b64 s[0:1], 0
